# phase I: LN2 weight and bias rows loaded once before the token loop instead of four reloads per token behind full vmcnt(0) drains
# speedup vs baseline: 1.0272x; 1.0042x over previous
.Li_tiles_done:
	s_load_dwordx2 s[12:13], s[0:1], 0x48
	s_load_dwordx2 s[10:11], s[0:1], 0x50
	s_load_dwordx2 s[14:15], s[0:1], 0x88
	s_load_dwordx2 s[18:19], s[0:1], 0x90
	s_load_dwordx2 s[8:9], s[0:1], 0x98
	s_lshl_b32 s39, s3, 3
	s_add_i32 s4, s29, s39
	s_cmpk_gt_i32 s4, 0x7fff
	s_cbranch_scc1 .LBB0_1281
	s_add_u32 s45, s6, 0x5d200000
	s_addc_u32 s54, s7, 0
	s_lshl_b32 s40, s74, 10
	s_lshl_b64 s[16:17], s[40:41], 2
	v_lshlrev_b32_e32 v30, 2, v2
	s_waitcnt lgkmcnt(0)
	s_add_u32 s12, s12, s16
	v_ashrrev_i32_e32 v31, 31, v30
	s_addc_u32 s13, s13, s17
	v_lshlrev_b64 v[14:15], 2, v[30:31]
	v_lshl_add_u64 v[6:7], s[12:13], 0, v[14:15]
	global_load_dwordx4 v[2:5], v[6:7], off
	s_add_u32 s10, s10, s16
	s_addc_u32 s11, s11, s17
	v_lshl_add_u64 v[8:9], s[10:11], 0, v[14:15]
	s_add_u32 s10, s6, 0x83200000
	s_addc_u32 s11, s7, 0
	s_add_u32 s40, s6, 0x94200000
	s_addc_u32 s56, s7, 0
	s_add_u32 s57, s6, 0x94300000
	s_addc_u32 s75, s7, 0
	s_add_u32 s80, s6, 0x94400000
	s_addc_u32 s81, s7, 0
	s_lshl_b32 s5, s24, 3
	s_add_u32 s82, s6, 0x3a200000
	s_addc_u32 s83, s7, 0
	s_lshl_b32 s59, s24, 4
	s_add_u32 s12, s6, 0x4d200000
	s_addc_u32 s13, s7, 0
	s_add_i32 s5, s4, s5
	s_min_i32 s20, s5, 0x7fff
	s_ashr_i32 s21, s20, 31
	s_lshl_b64 s[22:23], s[20:21], 11
	s_add_u32 s22, s12, s22
	s_addc_u32 s23, s13, s23
	v_lshlrev_b64 v[16:17], 1, v[30:31]
	v_lshl_add_u64 v[78:79], s[12:13], 0, v[16:17]
	s_mul_i32 s89, s24, 40
	s_waitcnt vmcnt(0)
	v_pk_mul_f32 v[32:33], v[4:5], s[66:67] op_sel_hi:[1,0]
	v_pk_mul_f32 v[34:35], v[2:3], s[66:67] op_sel_hi:[1,0]
	global_load_dwordx4 v[2:5], v[8:9], off
	s_waitcnt vmcnt(0)
	v_pk_mul_f32 v[36:37], v[4:5], s[66:67] op_sel_hi:[1,0]
	v_pk_mul_f32 v[38:39], v[2:3], s[66:67] op_sel_hi:[1,0]
	global_load_dwordx4 v[2:5], v[6:7], off offset:1024
	s_waitcnt vmcnt(0)
	v_pk_mul_f32 v[40:41], v[4:5], s[66:67] op_sel_hi:[1,0]
	v_pk_mul_f32 v[42:43], v[2:3], s[66:67] op_sel_hi:[1,0]
	global_load_dwordx4 v[2:5], v[8:9], off offset:1024
	s_waitcnt vmcnt(0)
	v_pk_mul_f32 v[44:45], v[4:5], s[66:67] op_sel_hi:[1,0]
	v_pk_mul_f32 v[46:47], v[2:3], s[66:67] op_sel_hi:[1,0]
	global_load_dwordx4 v[2:5], v[6:7], off offset:2048
	s_waitcnt vmcnt(0)
	v_pk_mul_f32 v[48:49], v[4:5], s[66:67] op_sel_hi:[1,0]
	v_pk_mul_f32 v[50:51], v[2:3], s[66:67] op_sel_hi:[1,0]
	global_load_dwordx4 v[2:5], v[8:9], off offset:2048
	s_waitcnt vmcnt(0)
	v_pk_mul_f32 v[52:53], v[4:5], s[66:67] op_sel_hi:[1,0]
	v_pk_mul_f32 v[54:55], v[2:3], s[66:67] op_sel_hi:[1,0]
	global_load_dwordx4 v[2:5], v[6:7], off offset:3072
	s_waitcnt vmcnt(0)
	v_pk_mul_f32 v[56:57], v[4:5], s[66:67] op_sel_hi:[1,0]
	v_pk_mul_f32 v[58:59], v[2:3], s[66:67] op_sel_hi:[1,0]
	global_load_dwordx4 v[2:5], v[8:9], off offset:3072
	s_waitcnt vmcnt(0)
	v_pk_mul_f32 v[62:63], v[2:3], s[66:67] op_sel_hi:[1,0]
	v_lshl_add_u64 v[2:3], s[22:23], 0, v[16:17]
	s_lshl_b64 s[22:23], s[20:21], 3
	s_add_u32 s22, s45, s22
	s_addc_u32 s23, s54, s23
	s_lshl_b32 s20, s20, 2
	s_ashr_i32 s21, s20, 31
	s_lshl_b64 s[20:21], s[20:21], 2
	global_load_dwordx2 v[64:65], v[2:3], off offset:1536
	global_load_dwordx2 v[72:73], v[2:3], off offset:1024
	global_load_dwordx2 v[74:75], v[2:3], off offset:512
	global_load_dwordx2 v[76:77], v[2:3], off
	global_load_dwordx2 v[70:71], v215, s[22:23]
	s_add_u32 s22, s40, s20
	s_addc_u32 s23, s56, s21
	v_pk_mul_f32 v[60:61], v[4:5], s[66:67] op_sel_hi:[1,0]
	global_load_dwordx4 v[2:5], v215, s[22:23]
	s_add_u32 s22, s80, s20
	s_addc_u32 s23, s81, s21
	s_add_u32 s20, s57, s20
	s_addc_u32 s21, s75, s21
	s_add_u32 s18, s18, s16
	s_addc_u32 s19, s19, s17
	s_ashr_i32 s5, s4, 31
	v_lshl_add_u64 v[82:83], s[18:19], 0, v[14:15]
	s_waitcnt vmcnt(0)
	v_lshlrev_b32_e32 v5, 2, v5
	v_add_u32_e32 v5, s38, v5
	ds_read_b32 v6, v5
	v_lshlrev_b32_e32 v4, 2, v4
	v_add_u32_e32 v4, s38, v4
	v_lshlrev_b32_e32 v3, 2, v3
	v_add_u32_e32 v3, s38, v3
	s_waitcnt lgkmcnt(0)
	v_ashrrev_i32_e32 v7, 31, v6
	v_lshlrev_b64 v[6:7], 18, v[6:7]
	v_lshl_add_u64 v[10:11], s[10:11], 0, v[6:7]
	global_load_dwordx4 v[6:9], v215, s[22:23]
	v_lshlrev_b32_e32 v2, 2, v2
	v_add_u32_e32 v2, s38, v2
	s_lshl_b64 s[22:23], s[4:5], 11
	s_waitcnt vmcnt(0)
	v_mov_b32_e32 v214, v9
	v_lshlrev_b64 v[12:13], 10, v[214:215]
	v_lshl_add_u64 v[10:11], v[10:11], 0, v[12:13]
	v_lshl_add_u64 v[10:11], v[10:11], 0, v[30:31]
	global_load_dword v122, v[10:11], off offset:768
	global_load_dword v123, v[10:11], off offset:512
	global_load_dword v124, v[10:11], off offset:256
	global_load_dword v125, v[10:11], off
	ds_read_b32 v4, v4
	v_mov_b32_e32 v9, v215
	v_lshlrev_b64 v[8:9], 10, v[8:9]
	v_mov_b32_e32 v214, v7
	v_mov_b32_e32 v7, v215
	s_waitcnt lgkmcnt(0)
	v_ashrrev_i32_e32 v5, 31, v4
	v_lshlrev_b64 v[4:5], 18, v[4:5]
	v_lshl_add_u64 v[4:5], s[10:11], 0, v[4:5]
	v_lshl_add_u64 v[4:5], v[4:5], 0, v[8:9]
	v_lshl_add_u64 v[4:5], v[4:5], 0, v[30:31]
	global_load_dword v118, v[4:5], off offset:768
	global_load_dword v119, v[4:5], off offset:512
	global_load_dword v120, v[4:5], off offset:256
	global_load_dword v121, v[4:5], off
	ds_read_b32 v4, v3
	v_lshlrev_b64 v[8:9], 10, v[214:215]
	s_waitcnt lgkmcnt(0)
	v_ashrrev_i32_e32 v5, 31, v4
	v_lshlrev_b64 v[4:5], 18, v[4:5]
	v_lshl_add_u64 v[4:5], s[10:11], 0, v[4:5]
	v_lshl_add_u64 v[4:5], v[4:5], 0, v[8:9]
	v_lshl_add_u64 v[4:5], v[4:5], 0, v[30:31]
	global_load_dword v114, v[4:5], off offset:768
	global_load_dword v115, v[4:5], off offset:512
	global_load_dword v116, v[4:5], off offset:256
	global_load_dword v117, v[4:5], off
	ds_read_b32 v2, v2
	v_lshlrev_b64 v[4:5], 10, v[6:7]
	s_waitcnt lgkmcnt(0)
	v_ashrrev_i32_e32 v3, 31, v2
	v_lshlrev_b64 v[2:3], 18, v[2:3]
	v_lshl_add_u64 v[2:3], s[10:11], 0, v[2:3]
	v_lshl_add_u64 v[2:3], v[2:3], 0, v[4:5]
	v_lshl_add_u64 v[2:3], v[2:3], 0, v[30:31]
	global_load_dword v110, v[2:3], off offset:768
	global_load_dword v111, v[2:3], off offset:512
	global_load_dword v112, v[2:3], off offset:256
	global_load_dword v113, v[2:3], off
	global_load_dwordx4 v[10:13], v215, s[20:21]
	s_add_u32 s20, s12, s22
	s_addc_u32 s21, s13, s23
	v_lshl_add_u64 v[2:3], s[20:21], 0, v[16:17]
	s_lshl_b64 s[20:21], s[4:5], 3
	s_add_u32 s20, s45, s20
	s_addc_u32 s21, s54, s21
	global_load_dwordx2 v[84:85], v[2:3], off offset:1536
	global_load_dwordx2 v[88:89], v[2:3], off offset:1024
	global_load_dwordx2 v[90:91], v[2:3], off offset:512
	global_load_dwordx2 v[92:93], v[2:3], off
	global_load_dwordx2 v[86:87], v215, s[20:21]
	s_add_u32 s20, s14, s16
	s_addc_u32 s21, s15, s17
	s_lshl_b32 s14, s4, 2
	s_ashr_i32 s15, s14, 31
	s_lshl_b64 s[14:15], s[14:15], 2
	s_add_u32 s16, s40, s14
	s_addc_u32 s17, s56, s15
	global_load_dwordx4 v[2:5], v215, s[16:17]
	s_add_u32 s16, s80, s14
	s_addc_u32 s17, s81, s15
	s_add_u32 s14, s57, s14
	s_addc_u32 s15, s75, s15
	v_and_b32_e32 v16, 64, v233
	v_add_u32_e32 v16, 64, v16
	v_xor_b32_e32 v17, 1, v233
	v_cmp_lt_i32_e32 vcc, v17, v16
	s_mul_i32 s12, s24, 24
	v_lshl_add_u64 v[80:81], s[20:21], 0, v[14:15]
	v_cndmask_b32_e32 v17, v233, v17, vcc
	v_lshlrev_b32_e32 v126, 2, v17
	v_xor_b32_e32 v17, 2, v233
	v_cmp_lt_i32_e32 vcc, v17, v16
	s_waitcnt vmcnt(0)
	v_lshlrev_b32_e32 v5, 2, v5
	v_add_u32_e32 v5, s38, v5
	ds_read_b32 v6, v5
	v_lshlrev_b32_e32 v4, 2, v4
	v_add_u32_e32 v4, s38, v4
	v_lshlrev_b32_e32 v3, 2, v3
	v_add_u32_e32 v3, s38, v3
	s_waitcnt lgkmcnt(0)
	v_ashrrev_i32_e32 v7, 31, v6
	v_lshlrev_b64 v[6:7], 18, v[6:7]
	v_lshl_add_u64 v[18:19], s[10:11], 0, v[6:7]
	global_load_dwordx4 v[6:9], v215, s[16:17]
	v_lshlrev_b32_e32 v2, 2, v2
	v_add_u32_e32 v2, s38, v2
	v_cndmask_b32_e32 v17, v233, v17, vcc
	v_lshlrev_b32_e32 v127, 2, v17
	v_xor_b32_e32 v17, 4, v233
	v_cmp_lt_i32_e32 vcc, v17, v16
	s_waitcnt vmcnt(0)
	v_mov_b32_e32 v214, v9
	v_lshlrev_b64 v[20:21], 10, v[214:215]
	v_lshl_add_u64 v[18:19], v[18:19], 0, v[20:21]
	v_lshl_add_u64 v[18:19], v[18:19], 0, v[30:31]
	global_load_dword v132, v[18:19], off offset:768
	global_load_dword v133, v[18:19], off offset:512
	global_load_dword v134, v[18:19], off offset:256
	global_load_dword v135, v[18:19], off
	ds_read_b32 v4, v4
	v_mov_b32_e32 v9, v215
	v_lshlrev_b64 v[8:9], 10, v[8:9]
	v_mov_b32_e32 v214, v7
	v_mov_b32_e32 v7, v215
	s_waitcnt lgkmcnt(0)
	v_ashrrev_i32_e32 v5, 31, v4
	v_lshlrev_b64 v[4:5], 18, v[4:5]
	v_lshl_add_u64 v[4:5], s[10:11], 0, v[4:5]
	v_lshl_add_u64 v[4:5], v[4:5], 0, v[8:9]
	v_lshl_add_u64 v[4:5], v[4:5], 0, v[30:31]
	global_load_dword v144, v[4:5], off offset:768
	global_load_dword v145, v[4:5], off offset:512
	global_load_dword v146, v[4:5], off offset:256
	global_load_dword v147, v[4:5], off
	ds_read_b32 v4, v3
	v_lshlrev_b64 v[8:9], 10, v[214:215]
	v_cndmask_b32_e32 v17, v233, v17, vcc
	v_lshlrev_b32_e32 v128, 2, v17
	v_xor_b32_e32 v17, 8, v233
	s_waitcnt lgkmcnt(0)
	v_ashrrev_i32_e32 v5, 31, v4
	v_lshlrev_b64 v[4:5], 18, v[4:5]
	v_lshl_add_u64 v[4:5], s[10:11], 0, v[4:5]
	v_lshl_add_u64 v[4:5], v[4:5], 0, v[8:9]
	v_lshl_add_u64 v[4:5], v[4:5], 0, v[30:31]
	global_load_dword v140, v[4:5], off offset:768
	global_load_dword v141, v[4:5], off offset:512
	global_load_dword v142, v[4:5], off offset:256
	global_load_dword v143, v[4:5], off
	ds_read_b32 v2, v2
	v_lshlrev_b64 v[4:5], 10, v[6:7]
	v_cmp_lt_i32_e32 vcc, v17, v16
	s_waitcnt lgkmcnt(0)
	v_ashrrev_i32_e32 v3, 31, v2
	v_lshlrev_b64 v[2:3], 18, v[2:3]
	v_lshl_add_u64 v[2:3], s[10:11], 0, v[2:3]
	v_lshl_add_u64 v[2:3], v[2:3], 0, v[4:5]
	v_lshl_add_u64 v[2:3], v[2:3], 0, v[30:31]
	global_load_dword v136, v[2:3], off offset:768
	global_load_dword v137, v[2:3], off offset:512
	global_load_dword v138, v[2:3], off offset:256
	global_load_dword v139, v[2:3], off
	v_cndmask_b32_e32 v17, v233, v17, vcc
	global_load_dwordx4 v[2:5], v215, s[14:15]
	s_add_i32 s14, s4, s59
	s_min_i32 s14, s14, 0x7fff
	s_lshl_b32 s14, s14, 2
	s_ashr_i32 s15, s14, 31
	s_lshl_b64 s[14:15], s[14:15], 2
	s_add_u32 s16, s57, s14
	s_addc_u32 s17, s75, s15
	global_load_dwordx4 v[6:9], v215, s[16:17]
	s_add_u32 s16, s80, s14
	s_addc_u32 s17, s81, s15
	s_add_u32 s14, s40, s14
	s_addc_u32 s15, s56, s15
	global_load_dwordx4 v[18:21], v215, s[16:17]
	global_load_dwordx4 v[22:25], v215, s[14:15]
	s_cmp_eq_u32 s74, 3
	s_cselect_b64 s[14:15], -1, 0
	s_cmp_lg_u32 s74, 3
	s_cselect_b64 s[16:17], -1, 0
	s_add_u32 s84, s6, 0x32200000
	s_addc_u32 s85, s7, 0
	s_lshl_b32 s60, s24, 5
	s_add_i32 s24, s24, s3
	s_add_i32 s89, s89, s39
	s_lshl_b32 s97, s24, 3
	s_add_i32 s60, s60, s39
	s_lshl_b64 s[6:7], s[4:5], 10
	v_lshlrev_b32_e32 v129, 2, v17
	v_xor_b32_e32 v17, 16, v233
	s_add_u32 s61, s84, s6
	v_cmp_lt_i32_e32 vcc, v17, v16
	s_addc_u32 s65, s85, s7
	s_ashr_i32 s13, s12, 31
	v_cndmask_b32_e32 v17, v233, v17, vcc
	s_lshl_b64 s[18:19], s[12:13], 10
	s_lshl_b64 s[4:5], s[4:5], 12
	v_lshlrev_b32_e32 v130, 2, v17
	v_xor_b32_e32 v17, 32, v233
	s_add_u32 s62, s8, s4
	v_cmp_lt_i32_e32 vcc, v17, v16
	s_addc_u32 s63, s9, s5
	s_lshl_b64 s[20:21], s[12:13], 12
	v_cndmask_b32_e32 v16, v233, v17, vcc
	s_add_u32 s33, s82, s22
	v_lshlrev_b32_e32 v131, 2, v16
	s_addc_u32 s3, s83, s23
	s_lshl_b64 s[22:23], s[12:13], 11
	s_add_i32 s13, s12, s39
	s_add_i32 s59, s59, s39
	global_load_dwordx4 v[174:177], v[80:81], off
	global_load_dwordx4 v[192:195], v[82:83], off
	global_load_dwordx4 v[178:181], v[80:81], off offset:1024
	global_load_dwordx4 v[196:199], v[82:83], off offset:1024
	global_load_dwordx4 v[182:185], v[80:81], off offset:2048
	global_load_dwordx4 v[202:205], v[82:83], off offset:2048
	global_load_dwordx4 v[186:189], v[80:81], off offset:3072
	global_load_dwordx4 v[206:209], v[82:83], off offset:3072
	s_branch .LBB0_1230

.LBB0_1230:
	s_waitcnt vmcnt(0)
	v_lshlrev_b32_e32 v14, 2, v22
	v_add_u32_e32 v14, s38, v14
	ds_read_b32 v14, v14
	v_lshlrev_b32_e32 v15, 2, v23
	v_lshlrev_b32_e32 v16, 2, v24
	v_add_u32_e32 v15, s38, v15
	v_add_u32_e32 v17, s38, v16
	v_lshlrev_b32_e32 v16, 2, v25
	v_add_u32_e32 v23, s38, v16
	ds_read_b32 v16, v15
	ds_read_b32 v22, v17
	ds_read_b32 v24, v23
	s_waitcnt lgkmcnt(3)
	v_ashrrev_i32_e32 v15, 31, v14
	v_mov_b32_e32 v214, v18
	v_lshlrev_b64 v[14:15], 18, v[14:15]
	s_waitcnt lgkmcnt(2)
	v_ashrrev_i32_e32 v17, 31, v16
	v_lshlrev_b64 v[26:27], 10, v[214:215]
	v_lshl_add_u64 v[14:15], s[10:11], 0, v[14:15]
	v_mov_b32_e32 v214, v19
	v_lshlrev_b64 v[16:17], 18, v[16:17]
	v_lshl_add_u64 v[14:15], v[14:15], 0, v[26:27]
	v_lshlrev_b64 v[18:19], 10, v[214:215]
	v_lshl_add_u64 v[16:17], s[10:11], 0, v[16:17]
	v_lshl_add_u64 v[14:15], v[14:15], 0, v[30:31]
	v_lshl_add_u64 v[16:17], v[16:17], 0, v[18:19]
	s_waitcnt lgkmcnt(1)
	v_ashrrev_i32_e32 v23, 31, v22
	v_lshl_add_u64 v[16:17], v[16:17], 0, v[30:31]
	global_load_dword v155, v[14:15], off
	global_load_dword v154, v[14:15], off offset:256
	global_load_dword v153, v[14:15], off offset:512
	global_load_dword v152, v[14:15], off offset:768
	global_load_dword v151, v[16:17], off
	global_load_dword v150, v[16:17], off offset:256
	global_load_dword v149, v[16:17], off offset:512
	global_load_dword v148, v[16:17], off offset:768
	v_mov_b32_e32 v214, v20
	v_lshlrev_b64 v[14:15], 18, v[22:23]
	v_lshlrev_b64 v[16:17], 10, v[214:215]
	v_lshl_add_u64 v[14:15], s[10:11], 0, v[14:15]
	s_waitcnt lgkmcnt(0)
	v_ashrrev_i32_e32 v25, 31, v24
	v_lshl_add_u64 v[14:15], v[14:15], 0, v[16:17]
	v_mov_b32_e32 v214, v21
	v_lshlrev_b64 v[16:17], 18, v[24:25]
	v_lshlrev_b64 v[18:19], 10, v[214:215]
	v_lshl_add_u64 v[16:17], s[10:11], 0, v[16:17]
	v_lshlrev_b32_e32 v28, 16, v88
	v_and_b32_e32 v29, 0xffff0000, v88
	v_lshlrev_b32_e32 v26, 16, v89
	v_and_b32_e32 v27, 0xffff0000, v89
	v_lshlrev_b32_e32 v88, 16, v84
	v_and_b32_e32 v89, 0xffff0000, v84
	v_lshl_add_u64 v[16:17], v[16:17], 0, v[18:19]
	v_lshlrev_b32_e32 v20, 16, v92
	v_and_b32_e32 v21, 0xffff0000, v92
	v_lshlrev_b32_e32 v18, 16, v93
	v_and_b32_e32 v19, 0xffff0000, v93
	v_lshlrev_b32_e32 v24, 16, v90
	v_and_b32_e32 v25, 0xffff0000, v90
	v_lshlrev_b32_e32 v22, 16, v91
	v_and_b32_e32 v23, 0xffff0000, v91
	v_lshlrev_b32_e32 v84, 16, v85
	v_and_b32_e32 v85, 0xffff0000, v85
	v_sub_f32_e32 v89, v89, v86
	v_sub_f32_e32 v88, v88, v86
	v_sub_f32_e32 v19, v19, v86
	v_sub_f32_e32 v18, v18, v86
	v_sub_f32_e32 v21, v21, v86
	v_sub_f32_e32 v20, v20, v86
	v_sub_f32_e32 v23, v23, v86
	v_sub_f32_e32 v22, v22, v86
	v_sub_f32_e32 v25, v25, v86
	v_sub_f32_e32 v24, v24, v86
	v_sub_f32_e32 v27, v27, v86
	v_sub_f32_e32 v26, v26, v86
	v_sub_f32_e32 v29, v29, v86
	v_sub_f32_e32 v28, v28, v86
	v_sub_f32_e32 v85, v85, v86
	v_sub_f32_e32 v84, v84, v86
	v_pk_mul_f32 v[88:89], v[86:87], v[88:89] op_sel:[1,0]
	v_pk_mul_f32 v[20:21], v[86:87], v[20:21] op_sel:[1,0]
	v_pk_mul_f32 v[18:19], v[86:87], v[18:19] op_sel:[1,0]
	v_pk_mul_f32 v[24:25], v[86:87], v[24:25] op_sel:[1,0]
	v_pk_mul_f32 v[22:23], v[86:87], v[22:23] op_sel:[1,0]
	v_pk_mul_f32 v[28:29], v[86:87], v[28:29] op_sel:[1,0]
	v_pk_mul_f32 v[26:27], v[86:87], v[26:27] op_sel:[1,0]
	v_pk_mul_f32 v[84:85], v[86:87], v[84:85] op_sel:[1,0]
	v_pk_fma_f32 v[86:87], v[58:59], v[88:89], v[62:63]
	v_cvt_pk_f32_fp8_e32 v[88:89], v139
	v_cvt_pk_f32_fp8_sdwa v[90:91], v139 src0_sel:WORD_1
	v_cvt_pk_f32_fp8_e32 v[92:93], v138
	v_cvt_pk_f32_fp8_sdwa v[94:95], v138 src0_sel:WORD_1
	v_pk_mul_f32 v[2:3], v[2:3], s[72:73] op_sel_hi:[1,0]
	v_pk_fma_f32 v[18:19], v[32:33], v[18:19], v[36:37]
	v_pk_fma_f32 v[20:21], v[34:35], v[20:21], v[38:39]
	v_pk_fma_f32 v[22:23], v[40:41], v[22:23], v[44:45]
	v_pk_fma_f32 v[24:25], v[42:43], v[24:25], v[46:47]
	v_pk_fma_f32 v[20:21], v[2:3], v[88:89], v[20:21] op_sel_hi:[0,1,1]
	v_pk_fma_f32 v[18:19], v[2:3], v[90:91], v[18:19] op_sel_hi:[0,1,1]
	v_pk_fma_f32 v[24:25], v[2:3], v[92:93], v[24:25] op_sel_hi:[0,1,1]
	v_pk_fma_f32 v[22:23], v[2:3], v[94:95], v[22:23] op_sel_hi:[0,1,1]
	v_cvt_pk_f32_fp8_e32 v[88:89], v137
	v_cvt_pk_f32_fp8_sdwa v[90:91], v137 src0_sel:WORD_1
	v_cvt_pk_f32_fp8_e32 v[92:93], v136
	v_cvt_pk_f32_fp8_sdwa v[94:95], v136 src0_sel:WORD_1
	v_pk_fma_f32 v[26:27], v[48:49], v[26:27], v[52:53]
	v_pk_fma_f32 v[28:29], v[50:51], v[28:29], v[54:55]
	v_pk_fma_f32 v[84:85], v[56:57], v[84:85], v[60:61]
	v_pk_fma_f32 v[28:29], v[2:3], v[88:89], v[28:29] op_sel_hi:[0,1,1]
	v_pk_fma_f32 v[26:27], v[2:3], v[90:91], v[26:27] op_sel_hi:[0,1,1]
	v_pk_fma_f32 v[86:87], v[2:3], v[92:93], v[86:87] op_sel_hi:[0,1,1]
	v_pk_fma_f32 v[84:85], v[2:3], v[94:95], v[84:85] op_sel_hi:[0,1,1]
	v_cvt_pk_f32_fp8_sdwa v[88:89], v143 src0_sel:WORD_1
	v_cvt_pk_f32_fp8_e32 v[90:91], v143
	v_cvt_pk_f32_fp8_sdwa v[92:93], v142 src0_sel:WORD_1
	v_cvt_pk_f32_fp8_e32 v[94:95], v142
	v_pk_fma_f32 v[18:19], v[2:3], v[88:89], v[18:19] op_sel:[1,0,0]
	v_pk_fma_f32 v[20:21], v[2:3], v[90:91], v[20:21] op_sel:[1,0,0]
	v_pk_fma_f32 v[22:23], v[2:3], v[92:93], v[22:23] op_sel:[1,0,0]
	v_pk_fma_f32 v[24:25], v[2:3], v[94:95], v[24:25] op_sel:[1,0,0]
	v_cvt_pk_f32_fp8_sdwa v[88:89], v141 src0_sel:WORD_1
	v_cvt_pk_f32_fp8_e32 v[90:91], v141
	v_cvt_pk_f32_fp8_sdwa v[92:93], v140 src0_sel:WORD_1
	v_cvt_pk_f32_fp8_e32 v[94:95], v140
	v_pk_fma_f32 v[26:27], v[2:3], v[88:89], v[26:27] op_sel:[1,0,0]
	v_pk_fma_f32 v[28:29], v[2:3], v[90:91], v[28:29] op_sel:[1,0,0]
	v_pk_fma_f32 v[84:85], v[2:3], v[92:93], v[84:85] op_sel:[1,0,0]
	v_pk_fma_f32 v[2:3], v[2:3], v[94:95], v[86:87] op_sel:[1,0,0]
	v_cvt_pk_f32_fp8_e32 v[86:87], v147
	v_cvt_pk_f32_fp8_sdwa v[88:89], v147 src0_sel:WORD_1
	v_cvt_pk_f32_fp8_e32 v[90:91], v146
	v_cvt_pk_f32_fp8_sdwa v[92:93], v146 src0_sel:WORD_1
	v_pk_mul_f32 v[4:5], v[4:5], s[72:73] op_sel_hi:[1,0]
	v_cvt_pk_f32_fp8_sdwa v[94:95], v132 src0_sel:WORD_1
	v_pk_fma_f32 v[20:21], v[4:5], v[86:87], v[20:21] op_sel_hi:[0,1,1]
	v_pk_fma_f32 v[18:19], v[4:5], v[88:89], v[18:19] op_sel_hi:[0,1,1]
	v_pk_fma_f32 v[86:87], v[4:5], v[90:91], v[24:25] op_sel_hi:[0,1,1]
	v_pk_fma_f32 v[88:89], v[4:5], v[92:93], v[22:23] op_sel_hi:[0,1,1]
	v_cvt_pk_f32_fp8_e32 v[22:23], v145
	v_cvt_pk_f32_fp8_sdwa v[24:25], v145 src0_sel:WORD_1
	v_cvt_pk_f32_fp8_e32 v[90:91], v144
	v_cvt_pk_f32_fp8_sdwa v[92:93], v144 src0_sel:WORD_1
	v_pk_fma_f32 v[28:29], v[4:5], v[22:23], v[28:29] op_sel_hi:[0,1,1]
	v_pk_fma_f32 v[26:27], v[4:5], v[24:25], v[26:27] op_sel_hi:[0,1,1]
	v_cvt_pk_f32_fp8_sdwa v[22:23], v135 src0_sel:WORD_1
	v_cvt_pk_f32_fp8_e32 v[24:25], v135
	v_pk_fma_f32 v[2:3], v[4:5], v[90:91], v[2:3] op_sel_hi:[0,1,1]
	v_pk_fma_f32 v[92:93], v[4:5], v[92:93], v[84:85] op_sel_hi:[0,1,1]
	v_cvt_pk_f32_fp8_sdwa v[84:85], v134 src0_sel:WORD_1
	v_cvt_pk_f32_fp8_e32 v[90:91], v134
	v_pk_fma_f32 v[22:23], v[4:5], v[22:23], v[18:19] op_sel:[1,0,0]
	v_pk_fma_f32 v[24:25], v[4:5], v[24:25], v[20:21] op_sel:[1,0,0]
	v_cvt_pk_f32_fp8_sdwa v[18:19], v133 src0_sel:WORD_1
	v_cvt_pk_f32_fp8_e32 v[20:21], v133
	v_cvt_pk_f32_fp8_e32 v[96:97], v132
	v_pk_fma_f32 v[88:89], v[4:5], v[84:85], v[88:89] op_sel:[1,0,0]
	v_pk_fma_f32 v[90:91], v[4:5], v[90:91], v[86:87] op_sel:[1,0,0]
	v_pk_fma_f32 v[84:85], v[4:5], v[18:19], v[26:27] op_sel:[1,0,0]
	v_pk_fma_f32 v[86:87], v[4:5], v[20:21], v[28:29] op_sel:[1,0,0]
	v_pk_fma_f32 v[26:27], v[4:5], v[94:95], v[92:93] op_sel:[1,0,0]
	v_pk_fma_f32 v[28:29], v[4:5], v[96:97], v[2:3] op_sel:[1,0,0]
	v_pk_mov_b32 v[2:3], v[24:25], v[22:23] op_sel:[1,0]
	v_mov_b32_e32 v4, v24
	v_mov_b32_e32 v5, v23
	v_pk_add_f32 v[2:3], v[2:3], v[4:5]
	v_pk_mov_b32 v[4:5], v[90:91], v[88:89] op_sel:[1,0]
	v_mov_b32_e32 v18, v90
	v_mov_b32_e32 v19, v89
	v_pk_add_f32 v[4:5], v[4:5], v[18:19]
	v_add_f32_e32 v2, v2, v3
	v_pk_add_f32 v[4:5], v[4:5], v[4:5] op_sel:[0,1] op_sel_hi:[1,0]
	v_add_f32_e32 v2, 0, v2
	v_add_f32_e32 v18, v86, v87
	v_add_f32_e32 v20, v84, v85
	v_mov_b32_e32 v3, v28
	v_mov_b32_e32 v5, v29
	v_mov_b32_e32 v19, v26
	v_mov_b32_e32 v21, v27
	v_pk_add_f32 v[2:3], v[2:3], v[4:5]
	v_pk_add_f32 v[4:5], v[18:19], v[20:21]
	s_add_i32 s24, s59, s29
	v_pk_add_f32 v[2:3], v[2:3], v[4:5]
	s_min_i32 s4, s24, 0x7fff
	v_add_f32_e32 v2, v2, v3
	ds_bpermute_b32 v3, v126, v2
	s_ashr_i32 s5, s4, 31
	s_lshl_b64 s[6:7], s[4:5], 3
	s_add_u32 s6, s45, s6
	s_addc_u32 s7, s54, s7
	s_waitcnt lgkmcnt(0)
	v_add_f32_e32 v4, v2, v3
	ds_bpermute_b32 v5, v127, v4
	s_lshl_b64 s[4:5], s[4:5], 11
	v_lshl_add_u64 v[14:15], v[14:15], 0, v[30:31]
	v_lshl_add_u64 v[2:3], v[78:79], 0, s[4:5]
	v_lshl_add_u64 v[16:17], v[16:17], 0, v[30:31]
	s_waitcnt lgkmcnt(0)
	v_add_f32_e32 v4, v4, v5
	ds_bpermute_b32 v5, v128, v4
	global_load_dword v163, v[14:15], off
	global_load_dword v162, v[14:15], off offset:256
	global_load_dword v161, v[14:15], off offset:512
	global_load_dword v160, v[14:15], off offset:768
	global_load_dword v159, v[16:17], off
	global_load_dword v158, v[16:17], off offset:256
	global_load_dword v157, v[16:17], off offset:512
	global_load_dword v156, v[16:17], off offset:768
	global_load_dwordx2 v[102:103], v[2:3], off
	global_load_dwordx2 v[100:101], v[2:3], off offset:512
	global_load_dwordx2 v[98:99], v[2:3], off offset:1024
	global_load_dwordx2 v[94:95], v[2:3], off offset:1536
	s_add_i32 s4, s13, s29
	s_min_i32 s26, s4, 0x7fff
	s_waitcnt lgkmcnt(0)
	v_add_f32_e32 v2, v4, v5
	ds_bpermute_b32 v3, v129, v2
	s_lshl_b32 s4, s26, 2
	s_ashr_i32 s5, s4, 31
	s_lshl_b64 s[76:77], s[4:5], 2
	s_add_u32 s4, s40, s76
	s_waitcnt lgkmcnt(0)
	v_add_f32_e32 v2, v2, v3
	ds_bpermute_b32 v3, v130, v2
	s_addc_u32 s5, s56, s77
	global_load_dwordx2 v[96:97], v215, s[6:7]
	global_load_dwordx4 v[14:17], v215, s[4:5]
	s_add_u32 s4, s80, s76
	s_addc_u32 s5, s81, s77
	s_waitcnt lgkmcnt(0)
	v_add_f32_e32 v2, v2, v3
	ds_bpermute_b32 v3, v131, v2
	s_add_u32 s6, s57, s76
	s_addc_u32 s7, s75, s77
	s_waitcnt lgkmcnt(0)
	v_add_f32_e32 v92, v2, v3
	v_fmamk_f32 v25, v92, 0xba800000, v25
	v_fmac_f32_e32 v24, 0xba800000, v92
	v_fmamk_f32 v23, v92, 0xba800000, v23
	v_fmac_f32_e32 v22, 0xba800000, v92
	v_pk_mul_f32 v[2:3], v[22:23], v[22:23]
	v_pk_mul_f32 v[4:5], v[24:25], v[24:25]
	v_fmamk_f32 v89, v92, 0xba800000, v89
	v_pk_mov_b32 v[18:19], v[4:5], v[2:3] op_sel:[1,0]
	v_mov_b32_e32 v5, v3
	v_pk_add_f32 v[2:3], v[18:19], v[4:5]
	v_fmac_f32_e32 v88, 0xba800000, v92
	v_fmamk_f32 v91, v92, 0xba800000, v91
	v_fmac_f32_e32 v90, 0xba800000, v92
	v_pk_add_f32 v[2:3], v[2:3], v[2:3] op_sel_hi:[0,1]
	v_pk_mul_f32 v[4:5], v[88:89], v[88:89]
	v_pk_mul_f32 v[18:19], v[90:91], v[90:91]
	v_fmac_f32_e32 v86, 0xba800000, v92
	v_pk_mov_b32 v[20:21], v[18:19], v[4:5] op_sel:[1,0]
	v_mov_b32_e32 v19, v5
	v_fmac_f32_e32 v84, 0xba800000, v92
	v_fmamk_f32 v87, v92, 0xba800000, v87
	v_mul_f32_e32 v2, v86, v86
	v_pk_add_f32 v[4:5], v[20:21], v[18:19]
	v_fmamk_f32 v85, v92, 0xba800000, v85
	v_pk_fma_f32 v[18:19], v[86:87], v[86:87], v[2:3] op_sel_hi:[1,1,0]
	v_mul_f32_e32 v2, v84, v84
	v_pk_add_f32 v[4:5], v[4:5], v[4:5] op_sel_hi:[0,1]
	v_pk_fma_f32 v[20:21], v[84:85], v[84:85], v[2:3] op_sel_hi:[1,1,0]
	v_fmamk_f32 v27, v92, 0xba800000, v27
	v_fmac_f32_e32 v26, 0xba800000, v92
	v_fmamk_f32 v29, v92, 0xba800000, v29
	v_fmac_f32_e32 v28, 0xba800000, v92
	v_mul_f32_e32 v18, v28, v28
	v_mul_f32_e32 v20, v29, v29
	v_mul_f32_e32 v2, v26, v26
	v_mul_f32_e32 v4, v27, v27
	v_pk_add_f32 v[18:19], v[18:19], v[20:21]
	v_pk_add_f32 v[2:3], v[2:3], v[4:5]
	s_nop 0
	v_pk_add_f32 v[2:3], v[18:19], v[2:3]
	s_nop 0
	v_add_f32_e32 v92, v2, v3
	global_load_dwordx4 v[18:21], v215, s[4:5]
	global_load_dwordx4 v[2:5], v215, s[6:7]
	ds_bpermute_b32 v93, v126, v92
	s_waitcnt lgkmcnt(0)
	v_add_f32_e32 v92, v92, v93
	ds_bpermute_b32 v93, v127, v92
	s_waitcnt lgkmcnt(0)
	v_add_f32_e32 v92, v92, v93
	ds_bpermute_b32 v93, v128, v92
	s_waitcnt lgkmcnt(0)
	v_add_f32_e32 v92, v92, v93
	ds_bpermute_b32 v93, v129, v92
	s_waitcnt lgkmcnt(0)
	v_add_f32_e32 v92, v92, v93
	ds_bpermute_b32 v93, v130, v92
	s_waitcnt lgkmcnt(0)
	v_add_f32_e32 v92, v92, v93
	ds_bpermute_b32 v93, v131, v92
	s_waitcnt lgkmcnt(0)
	v_add_f32_e32 v92, v92, v93
	v_fmamk_f32 v92, v92, 0x3a800000, v240
	v_mul_f32_e32 v93, 0x4f800000, v92
	v_cmp_gt_f32_e32 vcc, s36, v92
	s_nop 1
	v_cndmask_b32_e32 v92, v92, v93, vcc
	v_sqrt_f32_e32 v93, v92
	s_nop 0
	v_add_u32_e32 v104, -1, v93
	v_fma_f32 v105, -v104, v93, v92
	v_cmp_ge_f32_e64 s[4:5], 0, v105
	v_add_u32_e32 v105, 1, v93
	s_nop 0
	v_cndmask_b32_e64 v104, v93, v104, s[4:5]
	v_fma_f32 v93, -v105, v93, v92
	v_cmp_lt_f32_e64 s[4:5], 0, v93
	s_nop 1
	v_cndmask_b32_e64 v93, v104, v105, s[4:5]
	v_mul_f32_e32 v104, 0x37800000, v93
	v_cndmask_b32_e32 v93, v93, v104, vcc
	v_cmp_class_f32_e32 vcc, v92, v234
	s_and_b64 s[4:5], s[14:15], exec
	s_nop 0
	v_cndmask_b32_e32 v92, v93, v92, vcc
	v_div_scale_f32 v93, s[4:5], v92, v92, 1.0
	v_rcp_f32_e32 v104, v93
	s_cselect_b32 s5, s63, 0
	s_cselect_b32 s4, s62, 0
	s_cmp_lg_u64 s[4:5], 0
	v_fma_f32 v105, -v93, v104, 1.0
	v_fmac_f32_e32 v104, v105, v104
	v_div_scale_f32 v105, vcc, 1.0, v92, 1.0
	v_mul_f32_e32 v106, v105, v104
	v_fma_f32 v107, -v93, v106, v105
	v_fmac_f32_e32 v106, v107, v104
	v_fma_f32 v93, -v93, v106, v105
	v_div_fmas_f32 v93, v93, v104, v106
	v_div_fixup_f32 v106, v93, v92, 1.0
	v_pk_mul_f32 v[92:93], v[24:25], v[106:107] op_sel_hi:[1,0]
	v_pk_mul_f32 v[22:23], v[22:23], v[106:107] op_sel_hi:[1,0]
	s_cselect_b64 s[76:77], -1, 0
	s_cmp_eq_u64 s[4:5], 0
	v_lshl_add_u64 v[104:105], v[30:31], 2, s[4:5]
	s_waitcnt vmcnt(2)
	v_pk_fma_f32 v[24:25], v[176:177], v[22:23], v[194:195]
	v_pk_fma_f32 v[22:23], v[174:175], v[92:93], v[192:193]
	s_cbranch_scc1 .LBB0_1232
	global_store_dwordx4 v[104:105], v[22:25], off

.LBB0_1234:
	s_nop 0
	v_mov_b32_e32 v136, v106
	v_mov_b32_e32 v137, v106
	v_mov_b32_e32 v107, v106
	v_pk_mul_f32 v[88:89], v[88:89], v[136:137]
	v_pk_mul_f32 v[90:91], v[90:91], v[106:107]
	s_andn2_b64 vcc, exec, s[76:77]
	s_waitcnt vmcnt(0)
	v_pk_fma_f32 v[24:25], v[88:89], v[180:181], v[198:199]
	v_cndmask_b32_e64 v88, 0, 1, s[76:77]
	v_pk_fma_f32 v[22:23], v[90:91], v[178:179], v[196:197]
	v_cmp_ne_u32_e64 s[6:7], 1, v88
	s_cbranch_vccnz .LBB0_1236
	global_store_dwordx4 v[104:105], v[22:25], off offset:1024

.LBB0_1238:
	s_nop 0
	v_mov_b32_e32 v132, v106
	v_mov_b32_e32 v133, v106
	v_pk_mul_f32 v[86:87], v[86:87], v[106:107]
	v_pk_mul_f32 v[84:85], v[84:85], v[132:133]
	s_and_b64 vcc, exec, s[6:7]
	v_pk_fma_f32 v[24:25], v[84:85], v[184:185], v[204:205]
	v_pk_fma_f32 v[22:23], v[86:87], v[182:183], v[202:203]
	s_cbranch_vccnz .LBB0_1240
	global_store_dwordx4 v[104:105], v[22:25], off offset:2048

.LBB0_1242:
	s_nop 0
	v_mov_b32_e32 v88, v106
	v_mov_b32_e32 v89, v106
	v_pk_mul_f32 v[28:29], v[28:29], v[106:107]
	v_pk_mul_f32 v[26:27], v[26:27], v[88:89]
	s_and_b64 vcc, exec, s[6:7]
	v_pk_fma_f32 v[24:25], v[26:27], v[188:189], v[208:209]
	v_pk_fma_f32 v[22:23], v[28:29], v[186:187], v[206:207]
	s_cbranch_vccnz .LBB0_1244
	global_store_dwordx4 v[104:105], v[22:25], off offset:3072

.LBB0_1246:
	v_lshlrev_b32_e32 v14, 2, v14
	v_add_u32_e32 v14, s38, v14
	ds_read_b32 v22, v14
	v_mov_b32_e32 v214, v18
	v_lshlrev_b64 v[24:25], 10, v[214:215]
	v_lshlrev_b32_e32 v14, 2, v15
	v_add_u32_e32 v14, s38, v14
	s_waitcnt lgkmcnt(0)
	v_ashrrev_i32_e32 v23, 31, v22
	v_lshlrev_b64 v[22:23], 18, v[22:23]
	v_lshl_add_u64 v[22:23], s[10:11], 0, v[22:23]
	v_lshl_add_u64 v[22:23], v[22:23], 0, v[24:25]
	v_lshl_add_u64 v[22:23], v[22:23], 0, v[30:31]
	global_load_dword v139, v[22:23], off
	global_load_dword v138, v[22:23], off offset:256
	global_load_dword v137, v[22:23], off offset:512
	global_load_dword v136, v[22:23], off offset:768
	ds_read_b32 v14, v14
	v_mov_b32_e32 v214, v19
	v_lshlrev_b64 v[18:19], 10, v[214:215]
	v_mov_b32_e32 v214, v20
	s_ashr_i32 s27, s26, 31
	s_waitcnt lgkmcnt(0)
	v_ashrrev_i32_e32 v15, 31, v14
	v_lshlrev_b64 v[14:15], 18, v[14:15]
	v_lshl_add_u64 v[14:15], s[10:11], 0, v[14:15]
	v_lshl_add_u64 v[14:15], v[14:15], 0, v[18:19]
	v_lshl_add_u64 v[14:15], v[14:15], 0, v[30:31]
	global_load_dword v143, v[14:15], off
	global_load_dword v142, v[14:15], off offset:256
	global_load_dword v141, v[14:15], off offset:512
	global_load_dword v140, v[14:15], off offset:768
	v_lshlrev_b32_e32 v14, 2, v16
	v_add_u32_e32 v14, s38, v14
	ds_read_b32 v14, v14
	v_lshlrev_b64 v[18:19], 10, v[214:215]
	v_mov_b32_e32 v214, v21
	s_lshl_b64 s[6:7], s[26:27], 3
	s_add_u32 s6, s45, s6
	s_waitcnt lgkmcnt(0)
	v_ashrrev_i32_e32 v15, 31, v14
	v_lshlrev_b64 v[14:15], 18, v[14:15]
	v_lshl_add_u64 v[14:15], s[10:11], 0, v[14:15]
	v_lshl_add_u64 v[14:15], v[14:15], 0, v[18:19]
	v_lshl_add_u64 v[14:15], v[14:15], 0, v[30:31]
	global_load_dword v147, v[14:15], off
	global_load_dword v146, v[14:15], off offset:256
	global_load_dword v145, v[14:15], off offset:512
	global_load_dword v144, v[14:15], off offset:768
	v_lshlrev_b32_e32 v14, 2, v17
	v_add_u32_e32 v14, s38, v14
	ds_read_b32 v14, v14
	v_lshlrev_b64 v[16:17], 10, v[214:215]
	s_addc_u32 s7, s54, s7
	s_waitcnt lgkmcnt(0)
	v_ashrrev_i32_e32 v15, 31, v14
	v_lshlrev_b64 v[14:15], 18, v[14:15]
	v_lshl_add_u64 v[14:15], s[10:11], 0, v[14:15]
	v_lshl_add_u64 v[14:15], v[14:15], 0, v[16:17]
	v_lshl_add_u64 v[14:15], v[14:15], 0, v[30:31]
	global_load_dword v135, v[14:15], off
	global_load_dword v134, v[14:15], off offset:256
	global_load_dword v133, v[14:15], off offset:512
	global_load_dword v132, v[14:15], off offset:768
	global_load_dwordx2 v[86:87], v215, s[6:7]
	s_lshl_b64 s[6:7], s[26:27], 11
	v_lshl_add_u64 v[14:15], v[78:79], 0, s[6:7]
	s_add_i32 s6, s60, s29
	s_min_i32 s26, s6, 0x7fff
	s_lshl_b32 s6, s26, 2
	s_ashr_i32 s7, s6, 31
	s_lshl_b64 s[6:7], s[6:7], 2
	s_add_u32 s76, s40, s6
	s_addc_u32 s77, s56, s7
	global_load_dwordx2 v[92:93], v[14:15], off
	global_load_dwordx2 v[90:91], v[14:15], off offset:512
	global_load_dwordx2 v[88:89], v[14:15], off offset:1024
	global_load_dwordx2 v[84:85], v[14:15], off offset:1536
	global_load_dwordx4 v[22:25], v215, s[76:77]
	s_add_u32 s76, s80, s6
	s_addc_u32 s77, s81, s7
	s_add_u32 s6, s57, s6
	s_addc_u32 s7, s75, s7
	global_load_dwordx4 v[18:21], v215, s[76:77]
	global_load_dwordx4 v[14:17], v215, s[6:7]
	s_add_i32 s76, s97, s29
	s_cmpk_gt_i32 s76, 0x7fff
	s_cbranch_scc1 .LBB0_1263
	v_lshlrev_b32_e32 v106, 16, v64
	v_and_b32_e32 v107, 0xffff0000, v64
	v_lshlrev_b32_e32 v28, 16, v76
	v_and_b32_e32 v29, 0xffff0000, v76
	v_lshlrev_b32_e32 v26, 16, v77
	v_and_b32_e32 v27, 0xffff0000, v77
	v_lshlrev_b32_e32 v76, 16, v74
	v_and_b32_e32 v77, 0xffff0000, v74
	v_lshlrev_b32_e32 v74, 16, v75
	v_and_b32_e32 v75, 0xffff0000, v75
	v_lshlrev_b32_e32 v104, 16, v72
	v_and_b32_e32 v105, 0xffff0000, v72
	v_lshlrev_b32_e32 v72, 16, v73
	v_and_b32_e32 v73, 0xffff0000, v73
	v_lshlrev_b32_e32 v64, 16, v65
	v_and_b32_e32 v65, 0xffff0000, v65
	v_sub_f32_e32 v107, v107, v70
	v_sub_f32_e32 v106, v106, v70
	v_sub_f32_e32 v27, v27, v70
	v_sub_f32_e32 v26, v26, v70
	v_sub_f32_e32 v29, v29, v70
	v_sub_f32_e32 v28, v28, v70
	v_sub_f32_e32 v75, v75, v70
	v_sub_f32_e32 v74, v74, v70
	v_sub_f32_e32 v77, v77, v70
	v_sub_f32_e32 v76, v76, v70
	v_sub_f32_e32 v73, v73, v70
	v_sub_f32_e32 v72, v72, v70
	v_sub_f32_e32 v105, v105, v70
	v_sub_f32_e32 v104, v104, v70
	v_sub_f32_e32 v65, v65, v70
	v_sub_f32_e32 v64, v64, v70
	v_pk_mul_f32 v[106:107], v[70:71], v[106:107] op_sel:[1,0]
	v_pk_mul_f32 v[28:29], v[70:71], v[28:29] op_sel:[1,0]
	v_pk_mul_f32 v[26:27], v[70:71], v[26:27] op_sel:[1,0]
	v_pk_mul_f32 v[76:77], v[70:71], v[76:77] op_sel:[1,0]
	v_pk_mul_f32 v[74:75], v[70:71], v[74:75] op_sel:[1,0]
	v_pk_mul_f32 v[104:105], v[70:71], v[104:105] op_sel:[1,0]
	v_pk_mul_f32 v[72:73], v[70:71], v[72:73] op_sel:[1,0]
	v_pk_mul_f32 v[64:65], v[70:71], v[64:65] op_sel:[1,0]
	v_pk_fma_f32 v[70:71], v[58:59], v[106:107], v[62:63]
	v_cvt_pk_f32_fp8_e32 v[106:107], v113
	v_cvt_pk_f32_fp8_sdwa v[108:109], v113 src0_sel:WORD_1
	v_cvt_pk_f32_fp8_e32 v[164:165], v112
	v_cvt_pk_f32_fp8_sdwa v[112:113], v112 src0_sel:WORD_1
	v_pk_mul_f32 v[10:11], v[10:11], s[72:73] op_sel_hi:[1,0]
	v_pk_fma_f32 v[26:27], v[32:33], v[26:27], v[36:37]
	v_pk_fma_f32 v[28:29], v[34:35], v[28:29], v[38:39]
	v_pk_fma_f32 v[74:75], v[40:41], v[74:75], v[44:45]
	v_pk_fma_f32 v[28:29], v[10:11], v[106:107], v[28:29] op_sel_hi:[0,1,1]
	v_pk_fma_f32 v[26:27], v[10:11], v[108:109], v[26:27] op_sel_hi:[0,1,1]
	v_pk_fma_f32 v[74:75], v[10:11], v[112:113], v[74:75] op_sel_hi:[0,1,1]
	v_cvt_pk_f32_fp8_e32 v[106:107], v111
	v_cvt_pk_f32_fp8_sdwa v[108:109], v111 src0_sel:WORD_1
	v_cvt_pk_f32_fp8_e32 v[112:113], v110
	v_cvt_pk_f32_fp8_sdwa v[110:111], v110 src0_sel:WORD_1
	v_pk_fma_f32 v[72:73], v[48:49], v[72:73], v[52:53]
	v_pk_fma_f32 v[104:105], v[50:51], v[104:105], v[54:55]
	v_pk_fma_f32 v[64:65], v[56:57], v[64:65], v[60:61]
	v_pk_fma_f32 v[104:105], v[10:11], v[106:107], v[104:105] op_sel_hi:[0,1,1]
	v_pk_fma_f32 v[72:73], v[10:11], v[108:109], v[72:73] op_sel_hi:[0,1,1]
	v_pk_fma_f32 v[70:71], v[10:11], v[112:113], v[70:71] op_sel_hi:[0,1,1]
	v_pk_fma_f32 v[64:65], v[10:11], v[110:111], v[64:65] op_sel_hi:[0,1,1]
	v_cvt_pk_f32_fp8_sdwa v[106:107], v117 src0_sel:WORD_1
	v_cvt_pk_f32_fp8_e32 v[108:109], v117
	v_cvt_pk_f32_fp8_sdwa v[110:111], v116 src0_sel:WORD_1
	v_cvt_pk_f32_fp8_e32 v[112:113], v116
	v_pk_fma_f32 v[76:77], v[42:43], v[76:77], v[46:47]
	v_pk_fma_f32 v[26:27], v[10:11], v[106:107], v[26:27] op_sel:[1,0,0]
	v_pk_fma_f32 v[76:77], v[10:11], v[164:165], v[76:77] op_sel_hi:[0,1,1]
	v_pk_fma_f32 v[28:29], v[10:11], v[108:109], v[28:29] op_sel:[1,0,0]
	v_pk_fma_f32 v[74:75], v[10:11], v[110:111], v[74:75] op_sel:[1,0,0]
	v_pk_fma_f32 v[76:77], v[10:11], v[112:113], v[76:77] op_sel:[1,0,0]
	v_cvt_pk_f32_fp8_sdwa v[106:107], v115 src0_sel:WORD_1
	v_cvt_pk_f32_fp8_e32 v[108:109], v115
	v_cvt_pk_f32_fp8_sdwa v[110:111], v114 src0_sel:WORD_1
	v_cvt_pk_f32_fp8_e32 v[112:113], v114
	v_pk_fma_f32 v[72:73], v[10:11], v[106:107], v[72:73] op_sel:[1,0,0]
	v_pk_fma_f32 v[104:105], v[10:11], v[108:109], v[104:105] op_sel:[1,0,0]
	v_pk_fma_f32 v[64:65], v[10:11], v[110:111], v[64:65] op_sel:[1,0,0]
	v_pk_fma_f32 v[10:11], v[10:11], v[112:113], v[70:71] op_sel:[1,0,0]
	v_cvt_pk_f32_fp8_e32 v[70:71], v121
	v_cvt_pk_f32_fp8_sdwa v[106:107], v121 src0_sel:WORD_1
	v_cvt_pk_f32_fp8_e32 v[108:109], v120
	v_cvt_pk_f32_fp8_sdwa v[110:111], v120 src0_sel:WORD_1
	v_pk_mul_f32 v[12:13], v[12:13], s[72:73] op_sel_hi:[1,0]
	s_ashr_i32 s77, s76, 31
	v_pk_fma_f32 v[28:29], v[12:13], v[70:71], v[28:29] op_sel_hi:[0,1,1]
	v_pk_fma_f32 v[26:27], v[12:13], v[106:107], v[26:27] op_sel_hi:[0,1,1]
	v_pk_fma_f32 v[70:71], v[12:13], v[108:109], v[76:77] op_sel_hi:[0,1,1]
	v_pk_fma_f32 v[74:75], v[12:13], v[110:111], v[74:75] op_sel_hi:[0,1,1]
	v_cvt_pk_f32_fp8_e32 v[76:77], v119
	v_cvt_pk_f32_fp8_sdwa v[106:107], v119 src0_sel:WORD_1
	v_cvt_pk_f32_fp8_e32 v[108:109], v118
	v_cvt_pk_f32_fp8_sdwa v[110:111], v118 src0_sel:WORD_1
	v_pk_fma_f32 v[76:77], v[12:13], v[76:77], v[104:105] op_sel_hi:[0,1,1]
	v_pk_fma_f32 v[104:105], v[12:13], v[106:107], v[72:73] op_sel_hi:[0,1,1]
	v_pk_fma_f32 v[10:11], v[12:13], v[108:109], v[10:11] op_sel_hi:[0,1,1]
	v_pk_fma_f32 v[106:107], v[12:13], v[110:111], v[64:65] op_sel_hi:[0,1,1]
	v_cvt_pk_f32_fp8_sdwa v[64:65], v125 src0_sel:WORD_1
	v_cvt_pk_f32_fp8_e32 v[72:73], v125
	v_cvt_pk_f32_fp8_sdwa v[108:109], v124 src0_sel:WORD_1
	v_cvt_pk_f32_fp8_e32 v[110:111], v124
	v_pk_fma_f32 v[112:113], v[12:13], v[64:65], v[26:27] op_sel:[1,0,0]
	v_pk_fma_f32 v[114:115], v[12:13], v[72:73], v[28:29] op_sel:[1,0,0]
	v_pk_fma_f32 v[72:73], v[12:13], v[108:109], v[74:75] op_sel:[1,0,0]
	v_pk_fma_f32 v[74:75], v[12:13], v[110:111], v[70:71] op_sel:[1,0,0]
	v_cvt_pk_f32_fp8_sdwa v[26:27], v123 src0_sel:WORD_1
	v_cvt_pk_f32_fp8_e32 v[28:29], v123
	v_cvt_pk_f32_fp8_sdwa v[108:109], v122 src0_sel:WORD_1
	v_cvt_pk_f32_fp8_e32 v[110:111], v122
	v_pk_fma_f32 v[64:65], v[12:13], v[26:27], v[104:105] op_sel:[1,0,0]
	v_pk_fma_f32 v[70:71], v[12:13], v[28:29], v[76:77] op_sel:[1,0,0]
	v_pk_fma_f32 v[26:27], v[12:13], v[108:109], v[106:107] op_sel:[1,0,0]
	v_pk_fma_f32 v[28:29], v[12:13], v[110:111], v[10:11] op_sel:[1,0,0]
	v_pk_mov_b32 v[10:11], v[114:115], v[112:113] op_sel:[1,0]
	v_mov_b32_e32 v12, v114
	v_mov_b32_e32 v13, v113
	v_pk_add_f32 v[10:11], v[10:11], v[12:13]
	v_pk_mov_b32 v[12:13], v[74:75], v[72:73] op_sel:[1,0]
	v_mov_b32_e32 v76, v74
	v_mov_b32_e32 v77, v73
	v_pk_add_f32 v[12:13], v[12:13], v[76:77]
	v_add_f32_e32 v10, v10, v11
	v_pk_add_f32 v[12:13], v[12:13], v[12:13] op_sel:[0,1] op_sel_hi:[1,0]
	v_add_f32_e32 v10, 0, v10
	v_add_f32_e32 v76, v70, v71
	v_add_f32_e32 v104, v64, v65
	v_mov_b32_e32 v11, v28
	v_mov_b32_e32 v13, v29
	v_mov_b32_e32 v77, v26
	v_mov_b32_e32 v105, v27
	v_pk_add_f32 v[10:11], v[10:11], v[12:13]
	v_pk_add_f32 v[12:13], v[76:77], v[104:105]
	s_lshl_b64 s[6:7], s[76:77], 12
	v_pk_add_f32 v[10:11], v[10:11], v[12:13]
	s_add_u32 s25, s8, s6
	v_add_f32_e32 v10, v10, v11
	ds_bpermute_b32 v11, v126, v10
	s_addc_u32 s27, s9, s7
	s_waitcnt lgkmcnt(0)
	v_add_f32_e32 v10, v10, v11
	ds_bpermute_b32 v11, v127, v10
	s_waitcnt lgkmcnt(0)
	v_add_f32_e32 v10, v10, v11
	ds_bpermute_b32 v11, v128, v10
	s_waitcnt lgkmcnt(0)
	v_add_f32_e32 v10, v10, v11
	ds_bpermute_b32 v11, v129, v10
	s_waitcnt lgkmcnt(0)
	v_add_f32_e32 v10, v10, v11
	ds_bpermute_b32 v11, v130, v10
	s_waitcnt lgkmcnt(0)
	v_add_f32_e32 v10, v10, v11
	ds_bpermute_b32 v11, v131, v10
	s_waitcnt lgkmcnt(0)
	v_add_f32_e32 v106, v10, v11
	v_fmamk_f32 v115, v106, 0xba800000, v115
	v_fmac_f32_e32 v114, 0xba800000, v106
	v_fmamk_f32 v113, v106, 0xba800000, v113
	v_fmac_f32_e32 v112, 0xba800000, v106
	v_pk_mul_f32 v[10:11], v[112:113], v[112:113]
	v_pk_mul_f32 v[12:13], v[114:115], v[114:115]
	v_fmamk_f32 v73, v106, 0xba800000, v73
	v_pk_mov_b32 v[76:77], v[12:13], v[10:11] op_sel:[1,0]
	v_mov_b32_e32 v13, v11
	v_pk_add_f32 v[10:11], v[76:77], v[12:13]
	v_fmac_f32_e32 v72, 0xba800000, v106
	v_fmamk_f32 v75, v106, 0xba800000, v75
	v_fmac_f32_e32 v74, 0xba800000, v106
	v_pk_add_f32 v[10:11], v[10:11], v[10:11] op_sel_hi:[0,1]
	v_pk_mul_f32 v[12:13], v[72:73], v[72:73]
	v_pk_mul_f32 v[76:77], v[74:75], v[74:75]
	v_fmac_f32_e32 v70, 0xba800000, v106
	v_pk_mov_b32 v[104:105], v[76:77], v[12:13] op_sel:[1,0]
	v_mov_b32_e32 v77, v13
	v_fmac_f32_e32 v64, 0xba800000, v106
	v_fmamk_f32 v71, v106, 0xba800000, v71
	v_mul_f32_e32 v10, v70, v70
	v_pk_add_f32 v[12:13], v[104:105], v[76:77]
	v_fmamk_f32 v65, v106, 0xba800000, v65
	v_pk_fma_f32 v[76:77], v[70:71], v[70:71], v[10:11] op_sel_hi:[1,1,0]
	v_mul_f32_e32 v10, v64, v64
	v_pk_add_f32 v[12:13], v[12:13], v[12:13] op_sel_hi:[0,1]
	v_pk_fma_f32 v[104:105], v[64:65], v[64:65], v[10:11] op_sel_hi:[1,1,0]
	v_fmamk_f32 v27, v106, 0xba800000, v27
	v_fmac_f32_e32 v26, 0xba800000, v106
	v_fmamk_f32 v29, v106, 0xba800000, v29
	v_fmac_f32_e32 v28, 0xba800000, v106
	v_mul_f32_e32 v76, v28, v28
	v_mul_f32_e32 v104, v29, v29
	v_mul_f32_e32 v10, v26, v26
	v_mul_f32_e32 v12, v27, v27
	v_pk_add_f32 v[76:77], v[76:77], v[104:105]
	v_pk_add_f32 v[10:11], v[10:11], v[12:13]
	s_nop 0
	v_pk_add_f32 v[10:11], v[76:77], v[10:11]
	s_nop 0
	v_add_f32_e32 v76, v10, v11
	ds_bpermute_b32 v77, v126, v76
	s_waitcnt lgkmcnt(0)
	v_add_f32_e32 v76, v76, v77
	ds_bpermute_b32 v77, v127, v76
	s_waitcnt lgkmcnt(0)
	v_add_f32_e32 v76, v76, v77
	ds_bpermute_b32 v77, v128, v76
	s_waitcnt lgkmcnt(0)
	v_add_f32_e32 v76, v76, v77
	ds_bpermute_b32 v77, v129, v76
	s_waitcnt lgkmcnt(0)
	v_add_f32_e32 v76, v76, v77
	ds_bpermute_b32 v77, v130, v76
	s_waitcnt lgkmcnt(0)
	v_add_f32_e32 v76, v76, v77
	ds_bpermute_b32 v77, v131, v76
	s_waitcnt lgkmcnt(0)
	v_add_f32_e32 v76, v76, v77
	v_fmamk_f32 v76, v76, 0x3a800000, v240
	v_mul_f32_e32 v77, 0x4f800000, v76
	v_cmp_gt_f32_e32 vcc, s36, v76
	s_nop 1
	v_cndmask_b32_e32 v76, v76, v77, vcc
	v_sqrt_f32_e32 v77, v76
	s_nop 0
	v_add_u32_e32 v104, -1, v77
	v_fma_f32 v105, -v104, v77, v76
	v_cmp_ge_f32_e64 s[6:7], 0, v105
	v_add_u32_e32 v105, 1, v77
	s_nop 0
	v_cndmask_b32_e64 v104, v77, v104, s[6:7]
	v_fma_f32 v77, -v105, v77, v76
	v_cmp_lt_f32_e64 s[6:7], 0, v77
	s_nop 1
	v_cndmask_b32_e64 v77, v104, v105, s[6:7]
	v_mul_f32_e32 v104, 0x37800000, v77
	v_cndmask_b32_e32 v77, v77, v104, vcc
	v_cmp_class_f32_e32 vcc, v76, v234
	s_and_b64 s[6:7], s[14:15], exec
	s_nop 0
	v_cndmask_b32_e32 v76, v77, v76, vcc
	v_div_scale_f32 v77, s[6:7], v76, v76, 1.0
	v_rcp_f32_e32 v104, v77
	s_cselect_b32 s7, s27, 0
	s_cselect_b32 s6, s25, 0
	s_cmp_lg_u64 s[6:7], 0
	v_fma_f32 v105, -v77, v104, 1.0
	v_fmac_f32_e32 v104, v105, v104
	v_div_scale_f32 v105, vcc, 1.0, v76, 1.0
	v_mul_f32_e32 v106, v105, v104
	v_fma_f32 v107, -v77, v106, v105
	v_fmac_f32_e32 v106, v107, v104
	v_fma_f32 v77, -v77, v106, v105
	v_div_fmas_f32 v77, v77, v104, v106
	v_div_fixup_f32 v106, v77, v76, 1.0
	v_pk_mul_f32 v[76:77], v[114:115], v[106:107] op_sel_hi:[1,0]
	v_pk_mul_f32 v[112:113], v[112:113], v[106:107] op_sel_hi:[1,0]
	s_cselect_b64 s[78:79], -1, 0
	s_cmp_eq_u64 s[6:7], 0
	v_lshl_add_u64 v[104:105], v[30:31], 2, s[6:7]
	s_waitcnt vmcnt(0)
	v_pk_fma_f32 v[12:13], v[176:177], v[112:113], v[194:195]
	v_pk_fma_f32 v[10:11], v[174:175], v[76:77], v[192:193]
	s_cbranch_scc1 .LBB0_1249
	global_store_dwordx4 v[104:105], v[10:13], off

.LBB0_1251:
	s_nop 0
	v_mov_b32_e32 v114, v106
	v_mov_b32_e32 v115, v106
	v_mov_b32_e32 v107, v106
	v_pk_mul_f32 v[72:73], v[72:73], v[114:115]
	v_pk_mul_f32 v[74:75], v[74:75], v[106:107]
	s_andn2_b64 vcc, exec, s[78:79]
	v_pk_fma_f32 v[12:13], v[72:73], v[180:181], v[198:199]
	v_cndmask_b32_e64 v72, 0, 1, s[78:79]
	v_pk_fma_f32 v[10:11], v[74:75], v[178:179], v[196:197]
	v_cmp_ne_u32_e64 s[6:7], 1, v72
	s_cbranch_vccnz .LBB0_1253
	global_store_dwordx4 v[104:105], v[10:13], off offset:1024

.LBB0_1255:
	s_nop 0
	v_mov_b32_e32 v110, v106
	v_mov_b32_e32 v111, v106
	v_pk_mul_f32 v[70:71], v[70:71], v[106:107]
	v_pk_mul_f32 v[64:65], v[64:65], v[110:111]
	s_and_b64 vcc, exec, s[6:7]
	v_pk_fma_f32 v[12:13], v[64:65], v[184:185], v[204:205]
	v_pk_fma_f32 v[10:11], v[70:71], v[182:183], v[202:203]
	s_cbranch_vccnz .LBB0_1257
	global_store_dwordx4 v[104:105], v[10:13], off offset:2048

.LBB0_1259:
	s_nop 0
	v_mov_b32_e32 v64, v106
	v_mov_b32_e32 v65, v106
	v_pk_mul_f32 v[28:29], v[28:29], v[106:107]
	v_pk_mul_f32 v[26:27], v[26:27], v[64:65]
	s_and_b64 vcc, exec, s[6:7]
	v_pk_fma_f32 v[12:13], v[26:27], v[188:189], v[208:209]
	v_pk_fma_f32 v[10:11], v[28:29], v[186:187], v[206:207]
	s_cbranch_vccnz .LBB0_1261
	global_store_dwordx4 v[104:105], v[10:13], off offset:3072

.LBB0_1263:
	s_waitcnt vmcnt(2)
	v_lshlrev_b32_e32 v10, 2, v22
	v_add_u32_e32 v10, s38, v10
	ds_read_b32 v10, v10
	s_waitcnt vmcnt(1)
	v_mov_b32_e32 v214, v18
	v_lshlrev_b64 v[12:13], 10, v[214:215]
	v_mov_b32_e32 v214, v19
	s_ashr_i32 s27, s26, 31
	s_waitcnt lgkmcnt(0)
	v_ashrrev_i32_e32 v11, 31, v10
	v_lshlrev_b64 v[10:11], 18, v[10:11]
	v_lshl_add_u64 v[10:11], s[10:11], 0, v[10:11]
	v_lshl_add_u64 v[10:11], v[10:11], 0, v[12:13]
	v_lshl_add_u64 v[10:11], v[10:11], 0, v[30:31]
	global_load_dword v113, v[10:11], off
	global_load_dword v112, v[10:11], off offset:256
	global_load_dword v111, v[10:11], off offset:512
	global_load_dword v110, v[10:11], off offset:768
	v_lshlrev_b32_e32 v10, 2, v23
	v_add_u32_e32 v10, s38, v10
	ds_read_b32 v10, v10
	v_lshlrev_b64 v[12:13], 10, v[214:215]
	v_mov_b32_e32 v214, v20
	s_lshl_b64 s[6:7], s[26:27], 3
	s_add_u32 s6, s45, s6
	s_waitcnt lgkmcnt(0)
	v_ashrrev_i32_e32 v11, 31, v10
	v_lshlrev_b64 v[10:11], 18, v[10:11]
	v_lshl_add_u64 v[10:11], s[10:11], 0, v[10:11]
	v_lshl_add_u64 v[10:11], v[10:11], 0, v[12:13]
	v_lshl_add_u64 v[10:11], v[10:11], 0, v[30:31]
	global_load_dword v117, v[10:11], off
	global_load_dword v116, v[10:11], off offset:256
	global_load_dword v115, v[10:11], off offset:512
	global_load_dword v114, v[10:11], off offset:768
	v_lshlrev_b32_e32 v10, 2, v24
	v_add_u32_e32 v10, s38, v10
	ds_read_b32 v10, v10
	v_lshlrev_b64 v[12:13], 10, v[214:215]
	v_mov_b32_e32 v214, v21
	s_addc_u32 s7, s54, s7
	s_waitcnt lgkmcnt(0)
	v_ashrrev_i32_e32 v11, 31, v10
	v_lshlrev_b64 v[10:11], 18, v[10:11]
	v_lshl_add_u64 v[10:11], s[10:11], 0, v[10:11]
	v_lshl_add_u64 v[10:11], v[10:11], 0, v[12:13]
	v_lshl_add_u64 v[10:11], v[10:11], 0, v[30:31]
	global_load_dword v121, v[10:11], off
	global_load_dword v120, v[10:11], off offset:256
	global_load_dword v119, v[10:11], off offset:512
	global_load_dword v118, v[10:11], off offset:768
	v_lshlrev_b32_e32 v10, 2, v25
	v_add_u32_e32 v10, s38, v10
	ds_read_b32 v10, v10
	v_lshlrev_b64 v[12:13], 10, v[214:215]
	s_waitcnt lgkmcnt(0)
	v_ashrrev_i32_e32 v11, 31, v10
	v_lshlrev_b64 v[10:11], 18, v[10:11]
	v_lshl_add_u64 v[10:11], s[10:11], 0, v[10:11]
	v_lshl_add_u64 v[10:11], v[10:11], 0, v[12:13]
	v_lshl_add_u64 v[10:11], v[10:11], 0, v[30:31]
	global_load_dword v125, v[10:11], off
	global_load_dword v124, v[10:11], off offset:256
	global_load_dword v123, v[10:11], off offset:512
	global_load_dword v122, v[10:11], off offset:768
	global_load_dwordx2 v[70:71], v215, s[6:7]
	s_lshl_b64 s[6:7], s[26:27], 11
	v_lshl_add_u64 v[10:11], v[78:79], 0, s[6:7]
	s_add_i32 s6, s89, s29
	s_min_i32 s6, s6, 0x7fff
	s_lshl_b32 s6, s6, 2
	s_ashr_i32 s7, s6, 31
	s_lshl_b64 s[6:7], s[6:7], 2
	s_add_u32 s26, s40, s6
	s_addc_u32 s27, s56, s7
	global_load_dwordx2 v[76:77], v[10:11], off
	global_load_dwordx2 v[74:75], v[10:11], off offset:512
	global_load_dwordx2 v[72:73], v[10:11], off offset:1024
	global_load_dwordx2 v[64:65], v[10:11], off offset:1536
	global_load_dwordx4 v[22:25], v215, s[26:27]
	s_add_u32 s26, s80, s6
	s_addc_u32 s27, s81, s7
	s_add_u32 s6, s57, s6
	s_addc_u32 s7, s75, s7
	global_load_dwordx4 v[18:21], v215, s[26:27]
	global_load_dwordx4 v[26:29], v215, s[6:7]
	s_cmpk_gt_i32 s24, 0x7fff
	s_cbranch_scc1 .LBB0_1229
	v_lshlrev_b32_e32 v106, 16, v94
	v_and_b32_e32 v107, 0xffff0000, v94
	v_lshlrev_b32_e32 v12, 16, v102
	v_and_b32_e32 v13, 0xffff0000, v102
	v_lshlrev_b32_e32 v10, 16, v103
	v_and_b32_e32 v11, 0xffff0000, v103
	v_lshlrev_b32_e32 v102, 16, v100
	v_and_b32_e32 v103, 0xffff0000, v100
	v_lshlrev_b32_e32 v100, 16, v101
	v_and_b32_e32 v101, 0xffff0000, v101
	v_lshlrev_b32_e32 v104, 16, v98
	v_and_b32_e32 v105, 0xffff0000, v98
	v_lshlrev_b32_e32 v98, 16, v99
	v_and_b32_e32 v99, 0xffff0000, v99
	v_lshlrev_b32_e32 v94, 16, v95
	v_and_b32_e32 v95, 0xffff0000, v95
	v_sub_f32_e32 v107, v107, v96
	v_sub_f32_e32 v106, v106, v96
	v_sub_f32_e32 v11, v11, v96
	v_sub_f32_e32 v10, v10, v96
	v_sub_f32_e32 v13, v13, v96
	v_sub_f32_e32 v12, v12, v96
	v_sub_f32_e32 v101, v101, v96
	v_sub_f32_e32 v100, v100, v96
	v_sub_f32_e32 v103, v103, v96
	v_sub_f32_e32 v102, v102, v96
	v_sub_f32_e32 v99, v99, v96
	v_sub_f32_e32 v98, v98, v96
	v_sub_f32_e32 v105, v105, v96
	v_sub_f32_e32 v104, v104, v96
	v_sub_f32_e32 v95, v95, v96
	v_sub_f32_e32 v94, v94, v96
	v_pk_mul_f32 v[106:107], v[96:97], v[106:107] op_sel:[1,0]
	v_pk_mul_f32 v[12:13], v[96:97], v[12:13] op_sel:[1,0]
	v_pk_mul_f32 v[10:11], v[96:97], v[10:11] op_sel:[1,0]
	v_pk_mul_f32 v[102:103], v[96:97], v[102:103] op_sel:[1,0]
	v_pk_mul_f32 v[100:101], v[96:97], v[100:101] op_sel:[1,0]
	v_pk_mul_f32 v[104:105], v[96:97], v[104:105] op_sel:[1,0]
	v_pk_mul_f32 v[98:99], v[96:97], v[98:99] op_sel:[1,0]
	v_pk_mul_f32 v[94:95], v[96:97], v[94:95] op_sel:[1,0]
	v_pk_fma_f32 v[96:97], v[58:59], v[106:107], v[62:63]
	v_cvt_pk_f32_fp8_e32 v[106:107], v155
	v_cvt_pk_f32_fp8_sdwa v[108:109], v155 src0_sel:WORD_1
	v_cvt_pk_f32_fp8_e32 v[164:165], v154
	v_cvt_pk_f32_fp8_sdwa v[154:155], v154 src0_sel:WORD_1
	v_pk_mul_f32 v[6:7], v[6:7], s[72:73] op_sel_hi:[1,0]
	v_pk_fma_f32 v[10:11], v[32:33], v[10:11], v[36:37]
	v_pk_fma_f32 v[12:13], v[34:35], v[12:13], v[38:39]
	v_pk_fma_f32 v[100:101], v[40:41], v[100:101], v[44:45]
	v_pk_fma_f32 v[12:13], v[6:7], v[106:107], v[12:13] op_sel_hi:[0,1,1]
	v_pk_fma_f32 v[10:11], v[6:7], v[108:109], v[10:11] op_sel_hi:[0,1,1]
	v_pk_fma_f32 v[100:101], v[6:7], v[154:155], v[100:101] op_sel_hi:[0,1,1]
	v_cvt_pk_f32_fp8_e32 v[106:107], v153
	v_cvt_pk_f32_fp8_sdwa v[108:109], v153 src0_sel:WORD_1
	v_cvt_pk_f32_fp8_e32 v[154:155], v152
	v_cvt_pk_f32_fp8_sdwa v[152:153], v152 src0_sel:WORD_1
	v_pk_fma_f32 v[98:99], v[48:49], v[98:99], v[52:53]
	v_pk_fma_f32 v[104:105], v[50:51], v[104:105], v[54:55]
	v_pk_fma_f32 v[94:95], v[56:57], v[94:95], v[60:61]
	v_pk_fma_f32 v[104:105], v[6:7], v[106:107], v[104:105] op_sel_hi:[0,1,1]
	v_pk_fma_f32 v[98:99], v[6:7], v[108:109], v[98:99] op_sel_hi:[0,1,1]
	v_pk_fma_f32 v[94:95], v[6:7], v[152:153], v[94:95] op_sel_hi:[0,1,1]
	v_cvt_pk_f32_fp8_sdwa v[106:107], v151 src0_sel:WORD_1
	v_cvt_pk_f32_fp8_e32 v[108:109], v151
	v_cvt_pk_f32_fp8_sdwa v[152:153], v150 src0_sel:WORD_1
	v_cvt_pk_f32_fp8_e32 v[150:151], v150
	v_pk_fma_f32 v[102:103], v[42:43], v[102:103], v[46:47]
	v_pk_fma_f32 v[10:11], v[6:7], v[106:107], v[10:11] op_sel:[1,0,0]
	v_pk_fma_f32 v[102:103], v[6:7], v[164:165], v[102:103] op_sel_hi:[0,1,1]
	v_pk_fma_f32 v[12:13], v[6:7], v[108:109], v[12:13] op_sel:[1,0,0]
	v_pk_fma_f32 v[102:103], v[6:7], v[150:151], v[102:103] op_sel:[1,0,0]
	v_cvt_pk_f32_fp8_sdwa v[106:107], v149 src0_sel:WORD_1
	v_cvt_pk_f32_fp8_e32 v[108:109], v149
	v_cvt_pk_f32_fp8_sdwa v[150:151], v148 src0_sel:WORD_1
	v_cvt_pk_f32_fp8_e32 v[148:149], v148
	v_pk_fma_f32 v[96:97], v[6:7], v[154:155], v[96:97] op_sel_hi:[0,1,1]
	v_pk_fma_f32 v[100:101], v[6:7], v[152:153], v[100:101] op_sel:[1,0,0]
	v_pk_fma_f32 v[98:99], v[6:7], v[106:107], v[98:99] op_sel:[1,0,0]
	v_pk_fma_f32 v[104:105], v[6:7], v[108:109], v[104:105] op_sel:[1,0,0]
	v_pk_fma_f32 v[94:95], v[6:7], v[150:151], v[94:95] op_sel:[1,0,0]
	v_pk_fma_f32 v[6:7], v[6:7], v[148:149], v[96:97] op_sel:[1,0,0]
	v_cvt_pk_f32_fp8_e32 v[96:97], v163
	v_cvt_pk_f32_fp8_sdwa v[106:107], v163 src0_sel:WORD_1
	v_cvt_pk_f32_fp8_e32 v[108:109], v162
	v_cvt_pk_f32_fp8_sdwa v[148:149], v162 src0_sel:WORD_1
	v_pk_mul_f32 v[8:9], v[8:9], s[72:73] op_sel_hi:[1,0]
	s_ashr_i32 s25, s24, 31
	v_pk_fma_f32 v[12:13], v[8:9], v[96:97], v[12:13] op_sel_hi:[0,1,1]
	v_pk_fma_f32 v[10:11], v[8:9], v[106:107], v[10:11] op_sel_hi:[0,1,1]
	v_pk_fma_f32 v[96:97], v[8:9], v[108:109], v[102:103] op_sel_hi:[0,1,1]
	v_pk_fma_f32 v[100:101], v[8:9], v[148:149], v[100:101] op_sel_hi:[0,1,1]
	v_cvt_pk_f32_fp8_e32 v[102:103], v161
	v_cvt_pk_f32_fp8_sdwa v[106:107], v161 src0_sel:WORD_1
	v_cvt_pk_f32_fp8_e32 v[108:109], v160
	v_cvt_pk_f32_fp8_sdwa v[148:149], v160 src0_sel:WORD_1
	v_pk_fma_f32 v[102:103], v[8:9], v[102:103], v[104:105] op_sel_hi:[0,1,1]
	v_pk_fma_f32 v[104:105], v[8:9], v[106:107], v[98:99] op_sel_hi:[0,1,1]
	v_pk_fma_f32 v[6:7], v[8:9], v[108:109], v[6:7] op_sel_hi:[0,1,1]
	v_pk_fma_f32 v[106:107], v[8:9], v[148:149], v[94:95] op_sel_hi:[0,1,1]
	v_cvt_pk_f32_fp8_sdwa v[94:95], v159 src0_sel:WORD_1
	v_cvt_pk_f32_fp8_e32 v[98:99], v159
	v_cvt_pk_f32_fp8_sdwa v[108:109], v158 src0_sel:WORD_1
	v_cvt_pk_f32_fp8_e32 v[148:149], v158
	v_pk_fma_f32 v[152:153], v[8:9], v[94:95], v[10:11] op_sel:[1,0,0]
	v_pk_fma_f32 v[154:155], v[8:9], v[98:99], v[12:13] op_sel:[1,0,0]
	v_pk_fma_f32 v[98:99], v[8:9], v[108:109], v[100:101] op_sel:[1,0,0]
	v_pk_fma_f32 v[100:101], v[8:9], v[148:149], v[96:97] op_sel:[1,0,0]
	v_cvt_pk_f32_fp8_sdwa v[10:11], v157 src0_sel:WORD_1
	v_cvt_pk_f32_fp8_e32 v[12:13], v157
	v_cvt_pk_f32_fp8_sdwa v[108:109], v156 src0_sel:WORD_1
	v_cvt_pk_f32_fp8_e32 v[148:149], v156
	v_pk_fma_f32 v[94:95], v[8:9], v[10:11], v[104:105] op_sel:[1,0,0]
	v_pk_fma_f32 v[96:97], v[8:9], v[12:13], v[102:103] op_sel:[1,0,0]
	v_pk_fma_f32 v[10:11], v[8:9], v[108:109], v[106:107] op_sel:[1,0,0]
	v_pk_fma_f32 v[12:13], v[8:9], v[148:149], v[6:7] op_sel:[1,0,0]
	v_pk_mov_b32 v[6:7], v[154:155], v[152:153] op_sel:[1,0]
	v_mov_b32_e32 v8, v154
	v_mov_b32_e32 v9, v153
	v_pk_add_f32 v[6:7], v[6:7], v[8:9]
	v_pk_mov_b32 v[8:9], v[100:101], v[98:99] op_sel:[1,0]
	v_mov_b32_e32 v102, v100
	v_mov_b32_e32 v103, v99
	v_pk_add_f32 v[8:9], v[8:9], v[102:103]
	v_add_f32_e32 v6, v6, v7
	v_pk_add_f32 v[8:9], v[8:9], v[8:9] op_sel:[0,1] op_sel_hi:[1,0]
	v_add_f32_e32 v6, 0, v6
	v_add_f32_e32 v102, v96, v97
	v_add_f32_e32 v104, v94, v95
	v_mov_b32_e32 v7, v12
	v_mov_b32_e32 v9, v13
	v_mov_b32_e32 v103, v10
	v_mov_b32_e32 v105, v11
	v_pk_add_f32 v[6:7], v[6:7], v[8:9]
	v_pk_add_f32 v[8:9], v[102:103], v[104:105]
	s_lshl_b64 s[6:7], s[24:25], 12
	v_pk_add_f32 v[6:7], v[6:7], v[8:9]
	s_add_u32 s26, s8, s6
	v_add_f32_e32 v6, v6, v7
	ds_bpermute_b32 v7, v126, v6
	s_addc_u32 s27, s9, s7
	s_waitcnt lgkmcnt(0)
	v_add_f32_e32 v6, v6, v7
	ds_bpermute_b32 v7, v127, v6
	s_waitcnt lgkmcnt(0)
	v_add_f32_e32 v6, v6, v7
	ds_bpermute_b32 v7, v128, v6
	s_waitcnt lgkmcnt(0)
	v_add_f32_e32 v6, v6, v7
	ds_bpermute_b32 v7, v129, v6
	s_waitcnt lgkmcnt(0)
	v_add_f32_e32 v6, v6, v7
	ds_bpermute_b32 v7, v130, v6
	s_waitcnt lgkmcnt(0)
	v_add_f32_e32 v6, v6, v7
	ds_bpermute_b32 v7, v131, v6
	s_waitcnt lgkmcnt(0)
	v_add_f32_e32 v106, v6, v7
	v_fmamk_f32 v155, v106, 0xba800000, v155
	v_fmac_f32_e32 v154, 0xba800000, v106
	v_fmamk_f32 v153, v106, 0xba800000, v153
	v_fmac_f32_e32 v152, 0xba800000, v106
	v_pk_mul_f32 v[6:7], v[152:153], v[152:153]
	v_pk_mul_f32 v[8:9], v[154:155], v[154:155]
	v_fmamk_f32 v99, v106, 0xba800000, v99
	v_pk_mov_b32 v[102:103], v[8:9], v[6:7] op_sel:[1,0]
	v_mov_b32_e32 v9, v7
	v_pk_add_f32 v[6:7], v[102:103], v[8:9]
	v_fmac_f32_e32 v98, 0xba800000, v106
	v_fmamk_f32 v101, v106, 0xba800000, v101
	v_fmac_f32_e32 v100, 0xba800000, v106
	v_pk_add_f32 v[6:7], v[6:7], v[6:7] op_sel_hi:[0,1]
	v_pk_mul_f32 v[8:9], v[98:99], v[98:99]
	v_pk_mul_f32 v[102:103], v[100:101], v[100:101]
	v_fmac_f32_e32 v96, 0xba800000, v106
	v_pk_mov_b32 v[104:105], v[102:103], v[8:9] op_sel:[1,0]
	v_mov_b32_e32 v103, v9
	v_fmac_f32_e32 v94, 0xba800000, v106
	v_fmamk_f32 v97, v106, 0xba800000, v97
	v_mul_f32_e32 v6, v96, v96
	v_pk_add_f32 v[8:9], v[104:105], v[102:103]
	v_fmamk_f32 v95, v106, 0xba800000, v95
	v_pk_fma_f32 v[102:103], v[96:97], v[96:97], v[6:7] op_sel_hi:[1,1,0]
	v_mul_f32_e32 v6, v94, v94
	v_pk_add_f32 v[8:9], v[8:9], v[8:9] op_sel_hi:[0,1]
	v_pk_fma_f32 v[104:105], v[94:95], v[94:95], v[6:7] op_sel_hi:[1,1,0]
	v_fmamk_f32 v11, v106, 0xba800000, v11
	v_fmac_f32_e32 v10, 0xba800000, v106
	v_fmamk_f32 v13, v106, 0xba800000, v13
	v_fmac_f32_e32 v12, 0xba800000, v106
	v_mul_f32_e32 v102, v12, v12
	v_mul_f32_e32 v104, v13, v13
	v_mul_f32_e32 v6, v10, v10
	v_mul_f32_e32 v8, v11, v11
	v_pk_add_f32 v[102:103], v[102:103], v[104:105]
	v_pk_add_f32 v[6:7], v[6:7], v[8:9]
	s_nop 0
	v_pk_add_f32 v[6:7], v[102:103], v[6:7]
	s_nop 0
	v_add_f32_e32 v102, v6, v7
	ds_bpermute_b32 v103, v126, v102
	s_waitcnt lgkmcnt(0)
	v_add_f32_e32 v102, v102, v103
	ds_bpermute_b32 v103, v127, v102
	s_waitcnt lgkmcnt(0)
	v_add_f32_e32 v102, v102, v103
	ds_bpermute_b32 v103, v128, v102
	s_waitcnt lgkmcnt(0)
	v_add_f32_e32 v102, v102, v103
	ds_bpermute_b32 v103, v129, v102
	s_waitcnt lgkmcnt(0)
	v_add_f32_e32 v102, v102, v103
	ds_bpermute_b32 v103, v130, v102
	s_waitcnt lgkmcnt(0)
	v_add_f32_e32 v102, v102, v103
	ds_bpermute_b32 v103, v131, v102
	s_waitcnt lgkmcnt(0)
	v_add_f32_e32 v102, v102, v103
	v_fmamk_f32 v102, v102, 0x3a800000, v240
	v_mul_f32_e32 v103, 0x4f800000, v102
	v_cmp_gt_f32_e32 vcc, s36, v102
	s_nop 1
	v_cndmask_b32_e32 v102, v102, v103, vcc
	v_sqrt_f32_e32 v103, v102
	s_nop 0
	v_add_u32_e32 v104, -1, v103
	v_fma_f32 v105, -v104, v103, v102
	v_cmp_ge_f32_e64 s[6:7], 0, v105
	v_add_u32_e32 v105, 1, v103
	s_nop 0
	v_cndmask_b32_e64 v104, v103, v104, s[6:7]
	v_fma_f32 v103, -v105, v103, v102
	v_cmp_lt_f32_e64 s[6:7], 0, v103
	s_nop 1
	v_cndmask_b32_e64 v103, v104, v105, s[6:7]
	v_mul_f32_e32 v104, 0x37800000, v103
	v_cndmask_b32_e32 v103, v103, v104, vcc
	v_cmp_class_f32_e32 vcc, v102, v234
	s_and_b64 s[6:7], s[14:15], exec
	s_nop 0
	v_cndmask_b32_e32 v102, v103, v102, vcc
	v_div_scale_f32 v103, s[6:7], v102, v102, 1.0
	v_rcp_f32_e32 v104, v103
	s_cselect_b32 s7, s27, 0
	s_cselect_b32 s6, s26, 0
	s_cmp_lg_u64 s[6:7], 0
	v_fma_f32 v105, -v103, v104, 1.0
	v_fmac_f32_e32 v104, v105, v104
	v_div_scale_f32 v105, vcc, 1.0, v102, 1.0
	v_mul_f32_e32 v106, v105, v104
	v_fma_f32 v107, -v103, v106, v105
	v_fmac_f32_e32 v106, v107, v104
	v_fma_f32 v103, -v103, v106, v105
	v_div_fmas_f32 v103, v103, v104, v106
	v_div_fixup_f32 v106, v103, v102, 1.0
	v_pk_mul_f32 v[102:103], v[154:155], v[106:107] op_sel_hi:[1,0]
	v_pk_mul_f32 v[108:109], v[152:153], v[106:107] op_sel_hi:[1,0]
	s_cselect_b64 s[26:27], -1, 0
	s_cmp_eq_u64 s[6:7], 0
	v_lshl_add_u64 v[104:105], v[30:31], 2, s[6:7]
	s_waitcnt vmcnt(0)
	v_pk_fma_f32 v[8:9], v[176:177], v[108:109], v[194:195]
	v_pk_fma_f32 v[6:7], v[174:175], v[102:103], v[192:193]
	s_cbranch_scc1 .LBB0_1266
	global_store_dwordx4 v[104:105], v[6:9], off

.LBB0_1268:
	s_nop 0
	v_mov_b32_e32 v152, v106
	v_mov_b32_e32 v153, v106
	v_mov_b32_e32 v107, v106
	v_pk_mul_f32 v[98:99], v[98:99], v[152:153]
	v_pk_mul_f32 v[100:101], v[100:101], v[106:107]
	s_andn2_b64 vcc, exec, s[26:27]
	v_pk_fma_f32 v[8:9], v[98:99], v[180:181], v[198:199]
	v_cndmask_b32_e64 v98, 0, 1, s[26:27]
	v_pk_fma_f32 v[6:7], v[100:101], v[178:179], v[196:197]
	v_cmp_ne_u32_e64 s[6:7], 1, v98
	s_cbranch_vccnz .LBB0_1270
	global_store_dwordx4 v[104:105], v[6:9], off offset:1024

.LBB0_1272:
	s_nop 0
	v_mov_b32_e32 v148, v106
	v_mov_b32_e32 v149, v106
	v_pk_mul_f32 v[96:97], v[96:97], v[106:107]
	v_pk_mul_f32 v[94:95], v[94:95], v[148:149]
	s_and_b64 vcc, exec, s[6:7]
	v_pk_fma_f32 v[8:9], v[94:95], v[184:185], v[204:205]
	v_pk_fma_f32 v[6:7], v[96:97], v[182:183], v[202:203]
	s_cbranch_vccnz .LBB0_1274
	global_store_dwordx4 v[104:105], v[6:9], off offset:2048

.LBB0_1276:
	s_nop 0
	v_mov_b32_e32 v98, v106
	v_mov_b32_e32 v99, v106
	v_pk_mul_f32 v[12:13], v[12:13], v[106:107]
	v_pk_mul_f32 v[10:11], v[10:11], v[98:99]
	s_and_b64 vcc, exec, s[6:7]
	v_pk_fma_f32 v[8:9], v[10:11], v[188:189], v[208:209]
	v_pk_fma_f32 v[6:7], v[12:13], v[186:187], v[206:207]
	s_cbranch_vccnz .LBB0_1278
	global_store_dwordx4 v[104:105], v[6:9], off offset:3072
